# weight-prep: counted vmcnt ladders keep next item loads in flight; k-scale loads batched 2x dwordx4 ahead of data loads
# baseline (speedup 1.0000x reference)
.LBB0_39:
	v_add_u32_e32 v54, v132, v150
	v_add_u32_e32 v8, 8, v54
	v_add_u32_e32 v16, 16, v54
	v_add_u32_e32 v24, 24, v54
	v_add_u32_e32 v32, 32, v54
	v_add_u32_e32 v40, 40, v54
	v_ashrrev_i32_e32 v0, 31, v54
	v_ashrrev_i32_e32 v9, 31, v8
	v_ashrrev_i32_e32 v17, 31, v16
	v_ashrrev_i32_e32 v25, 31, v24
	v_ashrrev_i32_e32 v33, 31, v32
	v_ashrrev_i32_e32 v41, 31, v40
	v_add_u32_e32 v50, 48, v54
	v_mul_lo_u32 v2, s20, v0
	v_mul_lo_u32 v3, s21, v54
	v_mad_u64_u32 v[0:1], s[36:37], s20, v54, 0
	v_mul_lo_u32 v10, s20, v9
	v_mul_lo_u32 v11, s21, v8
	v_mad_u64_u32 v[8:9], s[36:37], s20, v8, 0
	v_mul_lo_u32 v18, s20, v17
	v_mul_lo_u32 v19, s21, v16
	v_mad_u64_u32 v[16:17], s[36:37], s20, v16, 0
	v_mul_lo_u32 v26, s20, v25
	v_mul_lo_u32 v27, s21, v24
	v_mad_u64_u32 v[24:25], s[36:37], s20, v24, 0
	v_mul_lo_u32 v34, s20, v33
	v_mul_lo_u32 v35, s21, v32
	v_mad_u64_u32 v[32:33], s[36:37], s20, v32, 0
	v_mul_lo_u32 v42, s20, v41
	v_mul_lo_u32 v43, s21, v40
	v_mad_u64_u32 v[40:41], s[36:37], s20, v40, 0
	v_ashrrev_i32_e32 v51, 31, v50
	v_add3_u32 v1, v1, v2, v3
	v_add_u32_e32 v2, 4, v54
	v_add3_u32 v9, v9, v10, v11
	v_add_u32_e32 v10, 12, v54
	v_add3_u32 v17, v17, v18, v19
	v_add_u32_e32 v18, 20, v54
	v_add3_u32 v25, v25, v26, v27
	v_add_u32_e32 v26, 28, v54
	v_add3_u32 v33, v33, v34, v35
	v_add_u32_e32 v34, 36, v54
	v_add3_u32 v41, v41, v42, v43
	v_add_u32_e32 v42, 44, v54
	v_mul_lo_u32 v52, s20, v51
	v_mul_lo_u32 v53, s21, v50
	v_mad_u64_u32 v[50:51], s[36:37], s20, v50, 0
	v_ashrrev_i32_e32 v3, 31, v2
	v_ashrrev_i32_e32 v11, 31, v10
	v_ashrrev_i32_e32 v19, 31, v18
	v_ashrrev_i32_e32 v27, 31, v26
	v_ashrrev_i32_e32 v35, 31, v34
	v_ashrrev_i32_e32 v43, 31, v42
	v_add3_u32 v51, v51, v52, v53
	v_add_u32_e32 v52, 52, v54
	v_mul_lo_u32 v4, s20, v3
	v_mul_lo_u32 v5, s21, v2
	v_mad_u64_u32 v[2:3], s[36:37], s20, v2, 0
	v_mul_lo_u32 v12, s20, v11
	v_mul_lo_u32 v13, s21, v10
	v_mad_u64_u32 v[10:11], s[36:37], s20, v10, 0
	v_mul_lo_u32 v20, s20, v19
	v_mul_lo_u32 v21, s21, v18
	v_mad_u64_u32 v[18:19], s[36:37], s20, v18, 0
	v_mul_lo_u32 v28, s20, v27
	v_mul_lo_u32 v29, s21, v26
	v_mad_u64_u32 v[26:27], s[36:37], s20, v26, 0
	v_mul_lo_u32 v36, s20, v35
	v_mul_lo_u32 v37, s21, v34
	v_mad_u64_u32 v[34:35], s[36:37], s20, v34, 0
	v_mul_lo_u32 v44, s20, v43
	v_mul_lo_u32 v45, s21, v42
	v_mad_u64_u32 v[42:43], s[36:37], s20, v42, 0
	v_ashrrev_i32_e32 v53, 31, v52
	v_add3_u32 v3, v3, v4, v5
	v_add3_u32 v11, v11, v12, v13
	v_add3_u32 v19, v19, v20, v21
	v_add3_u32 v27, v27, v28, v29
	v_add3_u32 v35, v35, v36, v37
	v_add3_u32 v43, v43, v44, v45
	v_mul_lo_u32 v55, s20, v53
	v_mul_lo_u32 v56, s21, v52
	v_mad_u64_u32 v[52:53], s[36:37], s20, v52, 0
	v_lshl_add_u64 v[0:1], v[0:1], 2, v[48:49]
	s_lshl_b32 s68, s46, 2
	s_ashr_i32 s43, s42, 31
	v_lshl_add_u64 v[2:3], v[2:3], 2, v[48:49]
	v_lshl_add_u64 v[8:9], v[8:9], 2, v[48:49]
	v_lshl_add_u64 v[10:11], v[10:11], 2, v[48:49]
	v_lshl_add_u64 v[16:17], v[16:17], 2, v[48:49]
	v_lshl_add_u64 v[18:19], v[18:19], 2, v[48:49]
	v_lshl_add_u64 v[24:25], v[24:25], 2, v[48:49]
	v_lshl_add_u64 v[26:27], v[26:27], 2, v[48:49]
	v_lshl_add_u64 v[32:33], v[32:33], 2, v[48:49]
	v_lshl_add_u64 v[34:35], v[34:35], 2, v[48:49]
	v_lshl_add_u64 v[40:41], v[40:41], 2, v[48:49]
	v_lshl_add_u64 v[42:43], v[42:43], 2, v[48:49]
	v_lshl_add_u64 v[50:51], v[50:51], 2, v[48:49]
	v_add3_u32 v53, v53, v55, v56
	v_lshl_add_u64 v[0:1], v[0:1], 0, s[68:69]
	s_lshl_b64 s[46:47], s[42:43], 2
	v_lshl_add_u64 v[2:3], v[2:3], 0, s[68:69]
	v_lshl_add_u64 v[8:9], v[8:9], 0, s[68:69]
	v_lshl_add_u64 v[10:11], v[10:11], 0, s[68:69]
	v_lshl_add_u64 v[16:17], v[16:17], 0, s[68:69]
	v_lshl_add_u64 v[18:19], v[18:19], 0, s[68:69]
	v_lshl_add_u64 v[24:25], v[24:25], 0, s[68:69]
	v_lshl_add_u64 v[26:27], v[26:27], 0, s[68:69]
	v_lshl_add_u64 v[32:33], v[32:33], 0, s[68:69]
	v_lshl_add_u64 v[34:35], v[34:35], 0, s[68:69]
	v_lshl_add_u64 v[40:41], v[40:41], 0, s[68:69]
	v_lshl_add_u64 v[42:43], v[42:43], 0, s[68:69]
	v_lshl_add_u64 v[50:51], v[50:51], 0, s[68:69]
	v_lshl_add_u64 v[52:53], v[52:53], 2, v[48:49]
	v_lshl_add_u64 v[0:1], v[0:1], 0, s[46:47]
	v_lshlrev_b32_e32 v208, 2, v151
	v_lshl_add_u64 v[2:3], v[2:3], 0, s[46:47]
	v_lshl_add_u64 v[8:9], v[8:9], 0, s[46:47]
	v_lshl_add_u64 v[10:11], v[10:11], 0, s[46:47]
	v_lshl_add_u64 v[16:17], v[16:17], 0, s[46:47]
	v_lshl_add_u64 v[18:19], v[18:19], 0, s[46:47]
	v_lshl_add_u64 v[24:25], v[24:25], 0, s[46:47]
	v_lshl_add_u64 v[26:27], v[26:27], 0, s[46:47]
	v_lshl_add_u64 v[32:33], v[32:33], 0, s[46:47]
	v_lshl_add_u64 v[34:35], v[34:35], 0, s[46:47]
	v_lshl_add_u64 v[40:41], v[40:41], 0, s[46:47]
	v_lshl_add_u64 v[42:43], v[42:43], 0, s[46:47]
	v_lshl_add_u64 v[50:51], v[50:51], 0, s[46:47]
	v_lshl_add_u64 v[52:53], v[52:53], 0, s[68:69]
	v_lshl_add_u64 v[0:1], v[0:1], 0, v[208:209]
	v_lshl_add_u64 v[4:5], v[2:3], 0, v[208:209]
	v_lshl_add_u64 v[8:9], v[8:9], 0, v[208:209]
	v_lshl_add_u64 v[12:13], v[10:11], 0, v[208:209]
	v_lshl_add_u64 v[16:17], v[16:17], 0, v[208:209]
	v_lshl_add_u64 v[20:21], v[18:19], 0, v[208:209]
	v_lshl_add_u64 v[24:25], v[24:25], 0, v[208:209]
	v_lshl_add_u64 v[28:29], v[26:27], 0, v[208:209]
	v_lshl_add_u64 v[32:33], v[32:33], 0, v[208:209]
	v_lshl_add_u64 v[36:37], v[34:35], 0, v[208:209]
	v_lshl_add_u64 v[40:41], v[40:41], 0, v[208:209]
	v_lshl_add_u64 v[44:45], v[42:43], 0, v[208:209]
	v_lshl_add_u64 v[50:51], v[50:51], 0, v[208:209]
	v_lshl_add_u64 v[52:53], v[52:53], 0, s[46:47]
	s_cmp_lg_u64 s[44:45], 0
	s_cselect_b32 s36, s44, s6
	s_cselect_b32 s37, s45, s7
	v_and_b32_e32 v248, 7, v200
	v_lshl_add_u32 v248, v248, 3, v132
	v_lshlrev_b32_e32 v248, 2, v248
	global_load_dwordx4 v[232:235], v248, s[36:37]
	global_load_dwordx4 v[236:239], v248, s[36:37] offset:16
	global_load_dwordx4 v[0:3], v[0:1], off
	s_nop 0
	global_load_dwordx4 v[4:7], v[4:5], off
	s_nop 0
	global_load_dwordx4 v[8:11], v[8:9], off
	s_nop 0
	global_load_dwordx4 v[12:15], v[12:13], off
	s_nop 0
	global_load_dwordx4 v[16:19], v[16:17], off
	s_nop 0
	global_load_dwordx4 v[20:23], v[20:21], off
	s_nop 0
	global_load_dwordx4 v[24:27], v[24:25], off
	s_nop 0
	global_load_dwordx4 v[28:31], v[28:29], off
	s_nop 0
	global_load_dwordx4 v[32:35], v[32:33], off
	s_nop 0
	global_load_dwordx4 v[36:39], v[36:37], off
	s_nop 0
	global_load_dwordx4 v[40:43], v[40:41], off
	s_nop 0
	global_load_dwordx4 v[44:47], v[44:45], off
	v_lshl_add_u64 v[52:53], v[52:53], 0, v[208:209]
	global_load_dwordx4 v[56:59], v[50:51], off
	global_load_dwordx4 v[60:63], v[52:53], off
	v_add_u32_e32 v50, 56, v54
	v_ashrrev_i32_e32 v51, 31, v50
	v_mul_lo_u32 v52, s20, v51
	v_mul_lo_u32 v53, s21, v50
	v_mad_u64_u32 v[50:51], s[36:37], s20, v50, 0
	v_add3_u32 v51, v51, v52, v53
	v_add_u32_e32 v52, 60, v54
	v_ashrrev_i32_e32 v53, 31, v52
	v_mul_lo_u32 v54, s20, v53
	v_mul_lo_u32 v55, s21, v52
	v_mad_u64_u32 v[52:53], s[20:21], s20, v52, 0
	v_lshl_add_u64 v[50:51], v[50:51], 2, v[48:49]
	v_add3_u32 v53, v53, v54, v55
	v_lshl_add_u64 v[50:51], v[50:51], 0, s[68:69]
	v_lshl_add_u64 v[48:49], v[52:53], 2, v[48:49]
	v_lshl_add_u64 v[50:51], v[50:51], 0, s[46:47]
	v_lshl_add_u64 v[48:49], v[48:49], 0, s[68:69]
	v_lshl_add_u64 v[50:51], v[50:51], 0, v[208:209]
	v_lshl_add_u64 v[48:49], v[48:49], 0, s[46:47]
	v_lshl_add_u64 v[48:49], v[48:49], 0, v[208:209]
	global_load_dwordx4 v[80:83], v[50:51], off
	global_load_dwordx4 v[84:87], v[48:49], off
	s_lshl_b32 s20, s25, 3
	s_andn2_b64 vcc, exec, s[0:1]
	v_and_b32_e32 v152, 7, v200
	s_cbranch_vccnz .LBB0_227

.LBB0_84:
	v_add_u32_e32 v122, s46, v150
	v_add_u32_e32 v64, 8, v122
	v_add_u32_e32 v72, 16, v122
	v_add_u32_e32 v88, 24, v122
	v_add_u32_e32 v96, 32, v122
	v_add_u32_e32 v104, 40, v122
	v_add_u32_e32 v112, 48, v122
	v_ashrrev_i32_e32 v48, 31, v122
	v_ashrrev_i32_e32 v65, 31, v64
	v_ashrrev_i32_e32 v73, 31, v72
	v_ashrrev_i32_e32 v89, 31, v88
	v_ashrrev_i32_e32 v97, 31, v96
	v_ashrrev_i32_e32 v105, 31, v104
	v_ashrrev_i32_e32 v113, 31, v112
	v_add_u32_e32 v120, 56, v122
	v_mul_lo_u32 v50, s56, v48
	v_mul_lo_u32 v51, s57, v122
	v_mad_u64_u32 v[48:49], s[60:61], s56, v122, 0
	v_mul_lo_u32 v66, s56, v65
	v_mul_lo_u32 v67, s57, v64
	v_mad_u64_u32 v[64:65], s[76:77], s56, v64, 0
	v_mul_lo_u32 v74, s56, v73
	v_mul_lo_u32 v75, s57, v72
	v_mad_u64_u32 v[72:73], s[76:77], s56, v72, 0
	v_mul_lo_u32 v90, s56, v89
	v_mul_lo_u32 v91, s57, v88
	v_mad_u64_u32 v[88:89], s[76:77], s56, v88, 0
	v_mul_lo_u32 v98, s56, v97
	v_mul_lo_u32 v99, s57, v96
	v_mad_u64_u32 v[96:97], s[76:77], s56, v96, 0
	v_mul_lo_u32 v106, s56, v105
	v_mul_lo_u32 v107, s57, v104
	v_mad_u64_u32 v[104:105], s[76:77], s56, v104, 0
	v_mul_lo_u32 v114, s56, v113
	v_mul_lo_u32 v115, s57, v112
	v_mad_u64_u32 v[112:113], s[76:77], s56, v112, 0
	v_ashrrev_i32_e32 v121, 31, v120
	v_add3_u32 v49, v49, v50, v51
	v_add_u32_e32 v50, 4, v122
	v_add3_u32 v65, v65, v66, v67
	v_add_u32_e32 v66, 12, v122
	v_add3_u32 v73, v73, v74, v75
	v_add_u32_e32 v74, 20, v122
	v_add3_u32 v89, v89, v90, v91
	v_add_u32_e32 v90, 28, v122
	v_add3_u32 v97, v97, v98, v99
	v_add_u32_e32 v98, 36, v122
	v_add3_u32 v105, v105, v106, v107
	v_add_u32_e32 v106, 44, v122
	v_add3_u32 v113, v113, v114, v115
	v_add_u32_e32 v114, 52, v122
	v_mul_lo_u32 v123, s56, v121
	v_mul_lo_u32 v124, s57, v120
	v_mad_u64_u32 v[120:121], s[76:77], s56, v120, 0
	v_add_u32_e32 v122, 60, v122
	v_ashrrev_i32_e32 v51, 31, v50
	v_ashrrev_i32_e32 v67, 31, v66
	v_ashrrev_i32_e32 v75, 31, v74
	v_ashrrev_i32_e32 v91, 31, v90
	v_ashrrev_i32_e32 v99, 31, v98
	v_ashrrev_i32_e32 v107, 31, v106
	v_ashrrev_i32_e32 v115, 31, v114
	v_add3_u32 v121, v121, v123, v124
	v_ashrrev_i32_e32 v123, 31, v122
	v_mul_lo_u32 v52, s56, v51
	v_mul_lo_u32 v53, s57, v50
	v_mad_u64_u32 v[50:51], s[76:77], s56, v50, 0
	v_mul_lo_u32 v68, s56, v67
	v_mul_lo_u32 v69, s57, v66
	v_mad_u64_u32 v[66:67], s[76:77], s56, v66, 0
	v_mul_lo_u32 v76, s56, v75
	v_mul_lo_u32 v77, s57, v74
	v_mad_u64_u32 v[74:75], s[76:77], s56, v74, 0
	v_mul_lo_u32 v92, s56, v91
	v_mul_lo_u32 v93, s57, v90
	v_mad_u64_u32 v[90:91], s[76:77], s56, v90, 0
	v_mul_lo_u32 v100, s56, v99
	v_mul_lo_u32 v101, s57, v98
	v_mad_u64_u32 v[98:99], s[76:77], s56, v98, 0
	v_mul_lo_u32 v108, s56, v107
	v_mul_lo_u32 v109, s57, v106
	v_mad_u64_u32 v[106:107], s[76:77], s56, v106, 0
	v_mul_lo_u32 v116, s56, v115
	v_mul_lo_u32 v117, s57, v114
	v_mad_u64_u32 v[114:115], s[76:77], s56, v114, 0
	v_mul_lo_u32 v124, s56, v123
	v_mul_lo_u32 v125, s57, v122
	v_mad_u64_u32 v[122:123], s[56:57], s56, v122, 0
	v_add3_u32 v51, v51, v52, v53
	v_add3_u32 v67, v67, v68, v69
	v_add3_u32 v75, v75, v76, v77
	v_add3_u32 v91, v91, v92, v93
	v_add3_u32 v99, v99, v100, v101
	v_add3_u32 v107, v107, v108, v109
	v_add3_u32 v115, v115, v116, v117
	v_add3_u32 v123, v123, v124, v125
	v_lshl_add_u64 v[48:49], v[48:49], 2, s[0:1]
	s_lshl_b64 s[58:59], s[58:59], 2
	s_ashr_i32 s51, s50, 31
	v_lshl_add_u64 v[50:51], v[50:51], 2, s[0:1]
	v_lshl_add_u64 v[64:65], v[64:65], 2, s[0:1]
	v_lshl_add_u64 v[66:67], v[66:67], 2, s[0:1]
	v_lshl_add_u64 v[72:73], v[72:73], 2, s[0:1]
	v_lshl_add_u64 v[74:75], v[74:75], 2, s[0:1]
	v_lshl_add_u64 v[88:89], v[88:89], 2, s[0:1]
	v_lshl_add_u64 v[90:91], v[90:91], 2, s[0:1]
	v_lshl_add_u64 v[96:97], v[96:97], 2, s[0:1]
	v_lshl_add_u64 v[98:99], v[98:99], 2, s[0:1]
	v_lshl_add_u64 v[104:105], v[104:105], 2, s[0:1]
	v_lshl_add_u64 v[106:107], v[106:107], 2, s[0:1]
	v_lshl_add_u64 v[112:113], v[112:113], 2, s[0:1]
	v_lshl_add_u64 v[114:115], v[114:115], 2, s[0:1]
	v_lshl_add_u64 v[120:121], v[120:121], 2, s[0:1]
	v_lshl_add_u64 v[122:123], v[122:123], 2, s[0:1]
	v_lshl_add_u64 v[48:49], v[48:49], 0, s[58:59]
	s_lshl_b64 s[60:61], s[50:51], 2
	v_lshl_add_u64 v[50:51], v[50:51], 0, s[58:59]
	v_lshl_add_u64 v[64:65], v[64:65], 0, s[58:59]
	v_lshl_add_u64 v[66:67], v[66:67], 0, s[58:59]
	v_lshl_add_u64 v[72:73], v[72:73], 0, s[58:59]
	v_lshl_add_u64 v[74:75], v[74:75], 0, s[58:59]
	v_lshl_add_u64 v[88:89], v[88:89], 0, s[58:59]
	v_lshl_add_u64 v[90:91], v[90:91], 0, s[58:59]
	v_lshl_add_u64 v[96:97], v[96:97], 0, s[58:59]
	v_lshl_add_u64 v[98:99], v[98:99], 0, s[58:59]
	v_lshl_add_u64 v[104:105], v[104:105], 0, s[58:59]
	v_lshl_add_u64 v[106:107], v[106:107], 0, s[58:59]
	v_lshl_add_u64 v[112:113], v[112:113], 0, s[58:59]
	v_lshl_add_u64 v[114:115], v[114:115], 0, s[58:59]
	v_lshl_add_u64 v[120:121], v[120:121], 0, s[58:59]
	v_lshl_add_u64 v[122:123], v[122:123], 0, s[58:59]
	v_lshl_add_u64 v[48:49], v[48:49], 0, s[60:61]
	v_lshlrev_b32_e32 v208, 2, v151
	v_lshl_add_u64 v[50:51], v[50:51], 0, s[60:61]
	v_lshl_add_u64 v[64:65], v[64:65], 0, s[60:61]
	v_lshl_add_u64 v[66:67], v[66:67], 0, s[60:61]
	v_lshl_add_u64 v[72:73], v[72:73], 0, s[60:61]
	v_lshl_add_u64 v[74:75], v[74:75], 0, s[60:61]
	v_lshl_add_u64 v[88:89], v[88:89], 0, s[60:61]
	v_lshl_add_u64 v[90:91], v[90:91], 0, s[60:61]
	v_lshl_add_u64 v[96:97], v[96:97], 0, s[60:61]
	v_lshl_add_u64 v[98:99], v[98:99], 0, s[60:61]
	v_lshl_add_u64 v[104:105], v[104:105], 0, s[60:61]
	v_lshl_add_u64 v[106:107], v[106:107], 0, s[60:61]
	v_lshl_add_u64 v[112:113], v[112:113], 0, s[60:61]
	v_lshl_add_u64 v[114:115], v[114:115], 0, s[60:61]
	v_lshl_add_u64 v[120:121], v[120:121], 0, s[60:61]
	v_lshl_add_u64 v[122:123], v[122:123], 0, s[60:61]
	v_lshl_add_u64 v[48:49], v[48:49], 0, v[208:209]
	v_lshl_add_u64 v[52:53], v[50:51], 0, v[208:209]
	v_lshl_add_u64 v[64:65], v[64:65], 0, v[208:209]
	v_lshl_add_u64 v[68:69], v[66:67], 0, v[208:209]
	v_lshl_add_u64 v[72:73], v[72:73], 0, v[208:209]
	v_lshl_add_u64 v[76:77], v[74:75], 0, v[208:209]
	v_lshl_add_u64 v[88:89], v[88:89], 0, v[208:209]
	v_lshl_add_u64 v[92:93], v[90:91], 0, v[208:209]
	v_lshl_add_u64 v[96:97], v[96:97], 0, v[208:209]
	v_lshl_add_u64 v[100:101], v[98:99], 0, v[208:209]
	v_lshl_add_u64 v[104:105], v[104:105], 0, v[208:209]
	v_lshl_add_u64 v[108:109], v[106:107], 0, v[208:209]
	v_lshl_add_u64 v[112:113], v[112:113], 0, v[208:209]
	v_lshl_add_u64 v[116:117], v[114:115], 0, v[208:209]
	v_lshl_add_u64 v[120:121], v[120:121], 0, v[208:209]
	v_lshl_add_u64 v[124:125], v[122:123], 0, v[208:209]
	s_cmp_lg_u64 s[52:53], 0
	s_cselect_b32 s60, s52, s6
	s_cselect_b32 s61, s53, s7
	v_add_u32_e32 v248, s46, v128
	v_lshlrev_b32_e32 v248, 2, v248
	global_load_dwordx4 v[240:243], v248, s[60:61]
	global_load_dwordx4 v[244:247], v248, s[60:61] offset:16
	global_load_dwordx4 v[48:51], v[48:49], off
	s_nop 0
	global_load_dwordx4 v[52:55], v[52:53], off
	s_nop 0
	global_load_dwordx4 v[64:67], v[64:65], off
	s_nop 0
	global_load_dwordx4 v[68:71], v[68:69], off
	s_nop 0
	global_load_dwordx4 v[72:75], v[72:73], off
	s_nop 0
	global_load_dwordx4 v[76:79], v[76:77], off
	s_nop 0
	global_load_dwordx4 v[88:91], v[88:89], off
	s_nop 0
	global_load_dwordx4 v[92:95], v[92:93], off
	s_nop 0
	global_load_dwordx4 v[96:99], v[96:97], off
	s_nop 0
	global_load_dwordx4 v[100:103], v[100:101], off
	s_nop 0
	global_load_dwordx4 v[104:107], v[104:105], off
	s_nop 0
	global_load_dwordx4 v[108:111], v[108:109], off
	s_nop 0
	global_load_dwordx4 v[112:115], v[112:113], off
	s_nop 0
	global_load_dwordx4 v[116:119], v[116:117], off
	s_nop 0
	global_load_dwordx4 v[120:123], v[120:121], off
	s_nop 0
	global_load_dwordx4 v[124:127], v[124:125], off
.LBB0_85:
	v_add_u32_e32 v164, 0x410, v162
	v_add_u32_e32 v165, 0x418, v162
	v_add_u32_e32 v166, 0x820, v162
	v_add_u32_e32 v167, 0x828, v162
	v_add_u32_e32 v168, 0xc30, v162
	v_add_u32_e32 v169, 0xc38, v162
	v_add_u32_e32 v170, 0x1040, v162
	v_add_u32_e32 v171, 0x1048, v162
	v_add_u32_e32 v172, 0x1450, v162
	v_add_u32_e32 v173, 0x1458, v162
	v_add_u32_e32 v174, 0x1860, v162
	v_add_u32_e32 v175, 0x1868, v162
	v_add_u32_e32 v176, 0x1c70, v162
	v_add_u32_e32 v177, 0x1c78, v162
	v_add_u32_e32 v178, 0x2080, v162
	v_add_u32_e32 v179, 0x2088, v162
	v_add_u32_e32 v180, 0x2490, v162
	v_add_u32_e32 v181, 0x2498, v162
	v_add_u32_e32 v182, 0x28a0, v162
	v_add_u32_e32 v183, 0x28a8, v162
	v_add_u32_e32 v184, 0x2cb0, v162
	v_add_u32_e32 v185, 0x2cb8, v162
	v_add_u32_e32 v186, 0x30c0, v162
	v_add_u32_e32 v187, 0x30c8, v162
	v_add_u32_e32 v188, 0x34d0, v162
	v_add_u32_e32 v189, 0x34d8, v162
	v_add_u32_e32 v190, 0x38e0, v162
	v_add_u32_e32 v191, 0x38e8, v162
	v_add_u32_e32 v192, 0x3cf0, v162
	v_add_u32_e32 v193, 0x3cf8, v162
	s_cmp_lg_u64 s[54:55], 0
	s_cbranch_scc0 .Lprep_wrA_last
	s_waitcnt vmcnt(33)
	ds_write2_b32 v162, v0, v1 offset1:1
	ds_write2_b32 v162, v2, v3 offset0:2 offset1:3
	s_waitcnt vmcnt(32)
	ds_write2_b32 v164, v4, v5 offset1:1
	ds_write2_b32 v165, v6, v7 offset1:1
	s_waitcnt vmcnt(31)
	ds_write2_b32 v166, v8, v9 offset1:1
	ds_write2_b32 v167, v10, v11 offset1:1
	s_waitcnt vmcnt(30)
	ds_write2_b32 v168, v12, v13 offset1:1
	ds_write2_b32 v169, v14, v15 offset1:1
	s_waitcnt vmcnt(29)
	ds_write2_b32 v170, v16, v17 offset1:1
	ds_write2_b32 v171, v18, v19 offset1:1
	s_waitcnt vmcnt(28)
	ds_write2_b32 v172, v20, v21 offset1:1
	ds_write2_b32 v173, v22, v23 offset1:1
	s_waitcnt vmcnt(27)
	ds_write2_b32 v174, v24, v25 offset1:1
	ds_write2_b32 v175, v26, v27 offset1:1
	s_waitcnt vmcnt(26)
	ds_write2_b32 v176, v28, v29 offset1:1
	ds_write2_b32 v177, v30, v31 offset1:1
	s_waitcnt vmcnt(25)
	ds_write2_b32 v178, v32, v33 offset1:1
	ds_write2_b32 v179, v34, v35 offset1:1
	s_waitcnt vmcnt(24)
	ds_write2_b32 v180, v36, v37 offset1:1
	ds_write2_b32 v181, v38, v39 offset1:1
	s_waitcnt vmcnt(23)
	ds_write2_b32 v182, v40, v41 offset1:1
	ds_write2_b32 v183, v42, v43 offset1:1
	s_waitcnt vmcnt(22)
	ds_write2_b32 v184, v44, v45 offset1:1
	ds_write2_b32 v185, v46, v47 offset1:1
	s_waitcnt vmcnt(21)
	ds_write2_b32 v186, v56, v57 offset1:1
	ds_write2_b32 v187, v58, v59 offset1:1
	s_waitcnt vmcnt(20)
	ds_write2_b32 v188, v60, v61 offset1:1
	ds_write2_b32 v189, v62, v63 offset1:1
	s_waitcnt vmcnt(19)
	ds_write2_b32 v190, v80, v81 offset1:1
	ds_write2_b32 v191, v82, v83 offset1:1
	s_waitcnt vmcnt(18)
	ds_write2_b32 v192, v84, v85 offset1:1
	ds_write2_b32 v193, v86, v87 offset1:1
	s_branch .Lprep_wrA_done
.Lprep_wrA_last:
	s_waitcnt vmcnt(15)
	ds_write2_b32 v162, v0, v1 offset1:1
	ds_write2_b32 v162, v2, v3 offset0:2 offset1:3
	s_waitcnt vmcnt(14)
	ds_write2_b32 v164, v4, v5 offset1:1
	ds_write2_b32 v165, v6, v7 offset1:1
	s_waitcnt vmcnt(13)
	ds_write2_b32 v166, v8, v9 offset1:1
	ds_write2_b32 v167, v10, v11 offset1:1
	s_waitcnt vmcnt(12)
	ds_write2_b32 v168, v12, v13 offset1:1
	ds_write2_b32 v169, v14, v15 offset1:1
	s_waitcnt vmcnt(11)
	ds_write2_b32 v170, v16, v17 offset1:1
	ds_write2_b32 v171, v18, v19 offset1:1
	s_waitcnt vmcnt(10)
	ds_write2_b32 v172, v20, v21 offset1:1
	ds_write2_b32 v173, v22, v23 offset1:1
	s_waitcnt vmcnt(9)
	ds_write2_b32 v174, v24, v25 offset1:1
	ds_write2_b32 v175, v26, v27 offset1:1
	s_waitcnt vmcnt(8)
	ds_write2_b32 v176, v28, v29 offset1:1
	ds_write2_b32 v177, v30, v31 offset1:1
	s_waitcnt vmcnt(7)
	ds_write2_b32 v178, v32, v33 offset1:1
	ds_write2_b32 v179, v34, v35 offset1:1
	s_waitcnt vmcnt(6)
	ds_write2_b32 v180, v36, v37 offset1:1
	ds_write2_b32 v181, v38, v39 offset1:1
	s_waitcnt vmcnt(5)
	ds_write2_b32 v182, v40, v41 offset1:1
	ds_write2_b32 v183, v42, v43 offset1:1
	s_waitcnt vmcnt(4)
	ds_write2_b32 v184, v44, v45 offset1:1
	ds_write2_b32 v185, v46, v47 offset1:1
	s_waitcnt vmcnt(3)
	ds_write2_b32 v186, v56, v57 offset1:1
	ds_write2_b32 v187, v58, v59 offset1:1
	s_waitcnt vmcnt(2)
	ds_write2_b32 v188, v60, v61 offset1:1
	ds_write2_b32 v189, v62, v63 offset1:1
	s_waitcnt vmcnt(1)
	ds_write2_b32 v190, v80, v81 offset1:1
	ds_write2_b32 v191, v82, v83 offset1:1
	s_waitcnt vmcnt(0)
	ds_write2_b32 v192, v84, v85 offset1:1
	ds_write2_b32 v193, v86, v87 offset1:1
.Lprep_wrA_done:
	s_waitcnt lgkmcnt(0)
	s_cmp_eq_u64 s[44:45], 0
	s_cbranch_scc1 .Lprep_ksA_none
	v_mul_f32_e32 v134, s73, v232
	v_mul_f32_e32 v135, s73, v233
	v_mul_f32_e32 v136, s73, v234
	v_mul_f32_e32 v137, s73, v235
	v_mul_f32_e32 v138, s73, v236
	v_mul_f32_e32 v139, s73, v237
	v_mul_f32_e32 v140, s73, v238
	v_mul_f32_e32 v141, s73, v239
	s_branch .LBB0_101
.Lprep_ksA_none:
	v_mov_b32_e32 v134, s73
	v_mov_b32_e32 v135, s73
	v_mov_b32_e32 v136, s73
	v_mov_b32_e32 v137, s73
	v_mov_b32_e32 v138, s73
	v_mov_b32_e32 v139, s73
	v_mov_b32_e32 v140, s73
	v_mov_b32_e32 v141, s73

.LBB0_177:
	v_add_u32_e32 v84, s51, v150
	v_add_u32_e32 v8, 8, v84
	v_add_u32_e32 v16, 16, v84
	v_add_u32_e32 v24, 24, v84
	v_add_u32_e32 v32, 32, v84
	v_add_u32_e32 v40, 40, v84
	v_add_u32_e32 v56, 48, v84
	v_ashrrev_i32_e32 v0, 31, v84
	v_ashrrev_i32_e32 v9, 31, v8
	v_ashrrev_i32_e32 v17, 31, v16
	v_ashrrev_i32_e32 v25, 31, v24
	v_ashrrev_i32_e32 v33, 31, v32
	v_ashrrev_i32_e32 v41, 31, v40
	v_ashrrev_i32_e32 v57, 31, v56
	v_add_u32_e32 v82, 56, v84
	v_mul_lo_u32 v2, s56, v0
	v_mul_lo_u32 v3, s57, v84
	v_mad_u64_u32 v[0:1], s[60:61], s56, v84, 0
	v_mul_lo_u32 v10, s56, v9
	v_mul_lo_u32 v11, s57, v8
	v_mad_u64_u32 v[8:9], s[76:77], s56, v8, 0
	v_mul_lo_u32 v18, s56, v17
	v_mul_lo_u32 v19, s57, v16
	v_mad_u64_u32 v[16:17], s[76:77], s56, v16, 0
	v_mul_lo_u32 v26, s56, v25
	v_mul_lo_u32 v27, s57, v24
	v_mad_u64_u32 v[24:25], s[76:77], s56, v24, 0
	v_mul_lo_u32 v34, s56, v33
	v_mul_lo_u32 v35, s57, v32
	v_mad_u64_u32 v[32:33], s[76:77], s56, v32, 0
	v_mul_lo_u32 v42, s56, v41
	v_mul_lo_u32 v43, s57, v40
	v_mad_u64_u32 v[40:41], s[76:77], s56, v40, 0
	v_mul_lo_u32 v58, s56, v57
	v_mul_lo_u32 v59, s57, v56
	v_mad_u64_u32 v[56:57], s[76:77], s56, v56, 0
	v_ashrrev_i32_e32 v83, 31, v82
	v_add3_u32 v1, v1, v2, v3
	v_add_u32_e32 v2, 4, v84
	v_add3_u32 v9, v9, v10, v11
	v_add_u32_e32 v10, 12, v84
	v_add3_u32 v17, v17, v18, v19
	v_add_u32_e32 v18, 20, v84
	v_add3_u32 v25, v25, v26, v27
	v_add_u32_e32 v26, 28, v84
	v_add3_u32 v33, v33, v34, v35
	v_add_u32_e32 v34, 36, v84
	v_add3_u32 v41, v41, v42, v43
	v_add_u32_e32 v42, 44, v84
	v_add3_u32 v57, v57, v58, v59
	v_add_u32_e32 v58, 52, v84
	v_mul_lo_u32 v85, s56, v83
	v_mul_lo_u32 v86, s57, v82
	v_mad_u64_u32 v[82:83], s[76:77], s56, v82, 0
	v_add_u32_e32 v84, 60, v84
	v_ashrrev_i32_e32 v3, 31, v2
	v_ashrrev_i32_e32 v11, 31, v10
	v_ashrrev_i32_e32 v19, 31, v18
	v_ashrrev_i32_e32 v27, 31, v26
	v_ashrrev_i32_e32 v35, 31, v34
	v_ashrrev_i32_e32 v43, 31, v42
	v_ashrrev_i32_e32 v59, 31, v58
	v_add3_u32 v83, v83, v85, v86
	v_ashrrev_i32_e32 v85, 31, v84
	v_mul_lo_u32 v4, s56, v3
	v_mul_lo_u32 v5, s57, v2
	v_mad_u64_u32 v[2:3], s[76:77], s56, v2, 0
	v_mul_lo_u32 v12, s56, v11
	v_mul_lo_u32 v13, s57, v10
	v_mad_u64_u32 v[10:11], s[76:77], s56, v10, 0
	v_mul_lo_u32 v20, s56, v19
	v_mul_lo_u32 v21, s57, v18
	v_mad_u64_u32 v[18:19], s[76:77], s56, v18, 0
	v_mul_lo_u32 v28, s56, v27
	v_mul_lo_u32 v29, s57, v26
	v_mad_u64_u32 v[26:27], s[76:77], s56, v26, 0
	v_mul_lo_u32 v36, s56, v35
	v_mul_lo_u32 v37, s57, v34
	v_mad_u64_u32 v[34:35], s[76:77], s56, v34, 0
	v_mul_lo_u32 v44, s56, v43
	v_mul_lo_u32 v45, s57, v42
	v_mad_u64_u32 v[42:43], s[76:77], s56, v42, 0
	v_mul_lo_u32 v60, s56, v59
	v_mul_lo_u32 v61, s57, v58
	v_mad_u64_u32 v[58:59], s[76:77], s56, v58, 0
	v_mul_lo_u32 v86, s56, v85
	v_mul_lo_u32 v87, s57, v84
	v_mad_u64_u32 v[84:85], s[56:57], s56, v84, 0
	v_add3_u32 v3, v3, v4, v5
	v_add3_u32 v11, v11, v12, v13
	v_add3_u32 v19, v19, v20, v21
	v_add3_u32 v27, v27, v28, v29
	v_add3_u32 v35, v35, v36, v37
	v_add3_u32 v43, v43, v44, v45
	v_add3_u32 v59, v59, v60, v61
	v_add3_u32 v85, v85, v86, v87
	v_lshl_add_u64 v[0:1], v[0:1], 2, s[0:1]
	s_lshl_b64 s[58:59], s[58:59], 2
	s_ashr_i32 s43, s42, 31
	v_lshl_add_u64 v[2:3], v[2:3], 2, s[0:1]
	v_lshl_add_u64 v[8:9], v[8:9], 2, s[0:1]
	v_lshl_add_u64 v[10:11], v[10:11], 2, s[0:1]
	v_lshl_add_u64 v[16:17], v[16:17], 2, s[0:1]
	v_lshl_add_u64 v[18:19], v[18:19], 2, s[0:1]
	v_lshl_add_u64 v[24:25], v[24:25], 2, s[0:1]
	v_lshl_add_u64 v[26:27], v[26:27], 2, s[0:1]
	v_lshl_add_u64 v[32:33], v[32:33], 2, s[0:1]
	v_lshl_add_u64 v[34:35], v[34:35], 2, s[0:1]
	v_lshl_add_u64 v[40:41], v[40:41], 2, s[0:1]
	v_lshl_add_u64 v[42:43], v[42:43], 2, s[0:1]
	v_lshl_add_u64 v[56:57], v[56:57], 2, s[0:1]
	v_lshl_add_u64 v[58:59], v[58:59], 2, s[0:1]
	v_lshl_add_u64 v[82:83], v[82:83], 2, s[0:1]
	v_lshl_add_u64 v[84:85], v[84:85], 2, s[0:1]
	v_lshl_add_u64 v[0:1], v[0:1], 0, s[58:59]
	s_lshl_b64 s[60:61], s[42:43], 2
	v_lshl_add_u64 v[2:3], v[2:3], 0, s[58:59]
	v_lshl_add_u64 v[8:9], v[8:9], 0, s[58:59]
	v_lshl_add_u64 v[10:11], v[10:11], 0, s[58:59]
	v_lshl_add_u64 v[16:17], v[16:17], 0, s[58:59]
	v_lshl_add_u64 v[18:19], v[18:19], 0, s[58:59]
	v_lshl_add_u64 v[24:25], v[24:25], 0, s[58:59]
	v_lshl_add_u64 v[26:27], v[26:27], 0, s[58:59]
	v_lshl_add_u64 v[32:33], v[32:33], 0, s[58:59]
	v_lshl_add_u64 v[34:35], v[34:35], 0, s[58:59]
	v_lshl_add_u64 v[40:41], v[40:41], 0, s[58:59]
	v_lshl_add_u64 v[42:43], v[42:43], 0, s[58:59]
	v_lshl_add_u64 v[56:57], v[56:57], 0, s[58:59]
	v_lshl_add_u64 v[58:59], v[58:59], 0, s[58:59]
	v_lshl_add_u64 v[82:83], v[82:83], 0, s[58:59]
	v_lshl_add_u64 v[84:85], v[84:85], 0, s[58:59]
	v_lshl_add_u64 v[0:1], v[0:1], 0, s[60:61]
	v_lshlrev_b32_e32 v80, 2, v151
	v_mov_b32_e32 v81, v209
	v_lshl_add_u64 v[2:3], v[2:3], 0, s[60:61]
	v_lshl_add_u64 v[8:9], v[8:9], 0, s[60:61]
	v_lshl_add_u64 v[10:11], v[10:11], 0, s[60:61]
	v_lshl_add_u64 v[16:17], v[16:17], 0, s[60:61]
	v_lshl_add_u64 v[18:19], v[18:19], 0, s[60:61]
	v_lshl_add_u64 v[24:25], v[24:25], 0, s[60:61]
	v_lshl_add_u64 v[26:27], v[26:27], 0, s[60:61]
	v_lshl_add_u64 v[32:33], v[32:33], 0, s[60:61]
	v_lshl_add_u64 v[34:35], v[34:35], 0, s[60:61]
	v_lshl_add_u64 v[40:41], v[40:41], 0, s[60:61]
	v_lshl_add_u64 v[42:43], v[42:43], 0, s[60:61]
	v_lshl_add_u64 v[56:57], v[56:57], 0, s[60:61]
	v_lshl_add_u64 v[58:59], v[58:59], 0, s[60:61]
	v_lshl_add_u64 v[82:83], v[82:83], 0, s[60:61]
	v_lshl_add_u64 v[84:85], v[84:85], 0, s[60:61]
	v_lshl_add_u64 v[0:1], v[0:1], 0, v[80:81]
	v_lshl_add_u64 v[4:5], v[2:3], 0, v[80:81]
	v_lshl_add_u64 v[8:9], v[8:9], 0, v[80:81]
	v_lshl_add_u64 v[12:13], v[10:11], 0, v[80:81]
	v_lshl_add_u64 v[16:17], v[16:17], 0, v[80:81]
	v_lshl_add_u64 v[20:21], v[18:19], 0, v[80:81]
	v_lshl_add_u64 v[24:25], v[24:25], 0, v[80:81]
	v_lshl_add_u64 v[28:29], v[26:27], 0, v[80:81]
	v_lshl_add_u64 v[32:33], v[32:33], 0, v[80:81]
	v_lshl_add_u64 v[36:37], v[34:35], 0, v[80:81]
	v_lshl_add_u64 v[40:41], v[40:41], 0, v[80:81]
	v_lshl_add_u64 v[44:45], v[42:43], 0, v[80:81]
	v_lshl_add_u64 v[56:57], v[56:57], 0, v[80:81]
	v_lshl_add_u64 v[60:61], v[58:59], 0, v[80:81]
	v_lshl_add_u64 v[82:83], v[82:83], 0, v[80:81]
	v_lshl_add_u64 v[84:85], v[84:85], 0, v[80:81]
	s_cmp_lg_u64 s[44:45], 0
	s_cselect_b32 s60, s44, s6
	s_cselect_b32 s61, s45, s7
	v_add_u32_e32 v248, s51, v128
	v_lshlrev_b32_e32 v248, 2, v248
	global_load_dwordx4 v[232:235], v248, s[60:61]
	global_load_dwordx4 v[236:239], v248, s[60:61] offset:16
	global_load_dwordx4 v[0:3], v[0:1], off
	s_nop 0
	global_load_dwordx4 v[4:7], v[4:5], off
	s_nop 0
	global_load_dwordx4 v[8:11], v[8:9], off
	s_nop 0
	global_load_dwordx4 v[12:15], v[12:13], off
	s_nop 0
	global_load_dwordx4 v[16:19], v[16:17], off
	s_nop 0
	global_load_dwordx4 v[20:23], v[20:21], off
	s_nop 0
	global_load_dwordx4 v[24:27], v[24:25], off
	s_nop 0
	global_load_dwordx4 v[28:31], v[28:29], off
	s_nop 0
	global_load_dwordx4 v[32:35], v[32:33], off
	s_nop 0
	global_load_dwordx4 v[36:39], v[36:37], off
	s_nop 0
	global_load_dwordx4 v[40:43], v[40:41], off
	s_nop 0
	global_load_dwordx4 v[44:47], v[44:45], off
	s_nop 0
	global_load_dwordx4 v[56:59], v[56:57], off
	s_nop 0
	global_load_dwordx4 v[60:63], v[60:61], off
	s_nop 0
	global_load_dwordx4 v[80:83], v[82:83], off
	s_nop 0
	global_load_dwordx4 v[84:87], v[84:85], off
	v_mov_b32_e32 v132, s51
	v_mov_b64_e32 v[130:131], s[54:55]
.LBB0_178:
	s_cmpk_gt_i32 s47, 0x213f
	s_cbranch_scc1 .Lprep_wrB_last
	s_waitcnt vmcnt(41)
	ds_write2_b32 v162, v48, v49 offset1:1
	ds_write2_b32 v162, v50, v51 offset0:2 offset1:3
	s_waitcnt vmcnt(40)
	ds_write2_b32 v164, v52, v53 offset1:1
	ds_write2_b32 v165, v54, v55 offset1:1
	s_waitcnt vmcnt(39)
	ds_write2_b32 v166, v64, v65 offset1:1
	ds_write2_b32 v167, v66, v67 offset1:1
	s_waitcnt vmcnt(38)
	ds_write2_b32 v168, v68, v69 offset1:1
	ds_write2_b32 v169, v70, v71 offset1:1
	s_waitcnt vmcnt(37)
	ds_write2_b32 v170, v72, v73 offset1:1
	ds_write2_b32 v171, v74, v75 offset1:1
	s_waitcnt vmcnt(36)
	ds_write2_b32 v172, v76, v77 offset1:1
	ds_write2_b32 v173, v78, v79 offset1:1
	s_waitcnt vmcnt(35)
	ds_write2_b32 v174, v88, v89 offset1:1
	ds_write2_b32 v175, v90, v91 offset1:1
	s_waitcnt vmcnt(34)
	ds_write2_b32 v176, v92, v93 offset1:1
	ds_write2_b32 v177, v94, v95 offset1:1
	s_waitcnt vmcnt(33)
	ds_write2_b32 v178, v96, v97 offset1:1
	ds_write2_b32 v179, v98, v99 offset1:1
	s_waitcnt vmcnt(32)
	ds_write2_b32 v180, v100, v101 offset1:1
	ds_write2_b32 v181, v102, v103 offset1:1
	s_waitcnt vmcnt(31)
	ds_write2_b32 v182, v104, v105 offset1:1
	ds_write2_b32 v183, v106, v107 offset1:1
	s_waitcnt vmcnt(30)
	ds_write2_b32 v184, v108, v109 offset1:1
	ds_write2_b32 v185, v110, v111 offset1:1
	s_waitcnt vmcnt(29)
	ds_write2_b32 v186, v112, v113 offset1:1
	ds_write2_b32 v187, v114, v115 offset1:1
	s_waitcnt vmcnt(28)
	ds_write2_b32 v188, v116, v117 offset1:1
	ds_write2_b32 v189, v118, v119 offset1:1
	s_waitcnt vmcnt(27)
	ds_write2_b32 v190, v120, v121 offset1:1
	ds_write2_b32 v191, v122, v123 offset1:1
	s_waitcnt vmcnt(26)
	ds_write2_b32 v192, v124, v125 offset1:1
	ds_write2_b32 v193, v126, v127 offset1:1
	s_branch .Lprep_wrB_done
.Lprep_wrB_last:
	s_waitcnt vmcnt(23)
	ds_write2_b32 v162, v48, v49 offset1:1
	ds_write2_b32 v162, v50, v51 offset0:2 offset1:3
	s_waitcnt vmcnt(22)
	ds_write2_b32 v164, v52, v53 offset1:1
	ds_write2_b32 v165, v54, v55 offset1:1
	s_waitcnt vmcnt(21)
	ds_write2_b32 v166, v64, v65 offset1:1
	ds_write2_b32 v167, v66, v67 offset1:1
	s_waitcnt vmcnt(20)
	ds_write2_b32 v168, v68, v69 offset1:1
	ds_write2_b32 v169, v70, v71 offset1:1
	s_waitcnt vmcnt(19)
	ds_write2_b32 v170, v72, v73 offset1:1
	ds_write2_b32 v171, v74, v75 offset1:1
	s_waitcnt vmcnt(18)
	ds_write2_b32 v172, v76, v77 offset1:1
	ds_write2_b32 v173, v78, v79 offset1:1
	s_waitcnt vmcnt(17)
	ds_write2_b32 v174, v88, v89 offset1:1
	ds_write2_b32 v175, v90, v91 offset1:1
	s_waitcnt vmcnt(16)
	ds_write2_b32 v176, v92, v93 offset1:1
	ds_write2_b32 v177, v94, v95 offset1:1
	s_waitcnt vmcnt(15)
	ds_write2_b32 v178, v96, v97 offset1:1
	ds_write2_b32 v179, v98, v99 offset1:1
	s_waitcnt vmcnt(14)
	ds_write2_b32 v180, v100, v101 offset1:1
	ds_write2_b32 v181, v102, v103 offset1:1
	s_waitcnt vmcnt(13)
	ds_write2_b32 v182, v104, v105 offset1:1
	ds_write2_b32 v183, v106, v107 offset1:1
	s_waitcnt vmcnt(12)
	ds_write2_b32 v184, v108, v109 offset1:1
	ds_write2_b32 v185, v110, v111 offset1:1
	s_waitcnt vmcnt(11)
	ds_write2_b32 v186, v112, v113 offset1:1
	ds_write2_b32 v187, v114, v115 offset1:1
	s_waitcnt vmcnt(10)
	ds_write2_b32 v188, v116, v117 offset1:1
	ds_write2_b32 v189, v118, v119 offset1:1
	s_waitcnt vmcnt(9)
	ds_write2_b32 v190, v120, v121 offset1:1
	ds_write2_b32 v191, v122, v123 offset1:1
	s_waitcnt vmcnt(8)
	ds_write2_b32 v192, v124, v125 offset1:1
	ds_write2_b32 v193, v126, v127 offset1:1
.Lprep_wrB_done:
	s_waitcnt lgkmcnt(0)
	s_cmp_eq_u64 s[52:53], 0
	s_cbranch_scc1 .Lprep_ksB_none
	v_mul_f32_e32 v134, s37, v240
	v_mul_f32_e32 v135, s37, v241
	v_mul_f32_e32 v136, s37, v242
	v_mul_f32_e32 v137, s37, v243
	v_mul_f32_e32 v138, s37, v244
	v_mul_f32_e32 v139, s37, v245
	v_mul_f32_e32 v140, s37, v246
	v_mul_f32_e32 v141, s37, v247
	s_branch .LBB0_194
.Lprep_ksB_none:
	v_mov_b32_e32 v134, s37
	v_mov_b32_e32 v135, s37
	v_mov_b32_e32 v136, s37
	v_mov_b32_e32 v137, s37
	v_mov_b32_e32 v138, s37
	v_mov_b32_e32 v139, s37
	v_mov_b32_e32 v140, s37
	v_mov_b32_e32 v141, s37
